# baseline (speedup 1.0000x reference)
_Z6gat_k1PKfS0_S0_S0_PDF16_S1_S1_Pf:
	s_load_dwordx8 s[4:11], s[0:1], 0x0
	s_load_dwordx8 s[12:19], s[0:1], 0x20
	v_lshrrev_b32_e32 v54, 6, v0
	v_bfe_u32 v123, v0, 4, 2
	v_and_b32_e32 v120, 15, v0
	v_lshlrev_b32_e32 v120, 4, v120
	v_lshl_or_b32 v120, v54, 8, v120
	v_mov_b32_e32 v121, 0
	v_and_b32_e32 v57, 0xc0, v0
	s_lshl_b32 s3, s2, 5
	v_and_b32_e32 v1, 63, v0
	v_bfe_u32 v55, v0, 5, 1
	v_lshlrev_b32_e32 v2, 8, v57
	v_mov_b32_e32 v19, 0
	v_or_b32_e32 v4, s3, v123
	v_and_b32_e32 v56, 31, v0
	v_lshl_or_b32 v18, v55, 11, v2
	v_lshlrev_b32_e32 v20, 4, v1
	v_mov_b32_e32 v21, v19
	v_ashrrev_i32_e32 v5, 31, v4
	s_waitcnt lgkmcnt(0)
	v_lshl_add_u64 v[2:3], s[6:7], 0, v[18:19]
	v_lshlrev_b32_e32 v18, 2, v56
	s_lshl_b32 s20, s3, 10
	s_add_u32 s20, s4, s20
	s_addc_u32 s21, s5, 0
	v_lshl_or_b32 v121, v123, 10, v120
	global_load_dwordx4 v[22:25], v121, s[20:21] nt
	s_add_u32 s20, s20, 0x1000
	s_addc_u32 s21, s21, 0
	global_load_dwordx4 v[26:29], v121, s[20:21] nt
	s_add_u32 s20, s20, 0x1000
	s_addc_u32 s21, s21, 0
	global_load_dwordx4 v[30:33], v121, s[20:21] nt
	s_add_u32 s20, s20, 0x1000
	s_addc_u32 s21, s21, 0
	global_load_dwordx4 v[34:37], v121, s[20:21] nt
	s_add_u32 s20, s20, 0x1000
	s_addc_u32 s21, s21, 0
	global_load_dwordx4 v[38:41], v121, s[20:21] nt
	s_add_u32 s20, s20, 0x1000
	s_addc_u32 s21, s21, 0
	global_load_dwordx4 v[42:45], v121, s[20:21] nt
	s_add_u32 s20, s20, 0x1000
	s_addc_u32 s21, s21, 0
	global_load_dwordx4 v[46:49], v121, s[20:21] nt
	s_add_u32 s20, s20, 0x1000
	s_addc_u32 s21, s21, 0
	global_load_dwordx4 v[50:53], v121, s[20:21] nt
	s_movk_i32 s4, 0x410
	v_mad_u32_u24 v122, v123, s4, v120
	v_lshl_add_u64 v[2:3], v[2:3], 0, v[18:19]
	global_load_dword v58, v[2:3], off
	global_load_dword v59, v[2:3], off offset:128
	global_load_dword v60, v[2:3], off offset:256
	global_load_dword v61, v[2:3], off offset:384
	global_load_dword v62, v[2:3], off offset:512
	global_load_dword v63, v[2:3], off offset:640
	global_load_dword v64, v[2:3], off offset:768
	global_load_dword v65, v[2:3], off offset:896
	global_load_dword v19, v[2:3], off offset:1024
	global_load_dword v66, v[2:3], off offset:1152
	global_load_dword v67, v[2:3], off offset:1280
	global_load_dword v68, v[2:3], off offset:1408
	global_load_dword v69, v[2:3], off offset:1536
	global_load_dword v70, v[2:3], off offset:1664
	global_load_dword v71, v[2:3], off offset:1792
	global_load_dword v72, v[2:3], off offset:1920
	s_movk_i32 s4, 0x1000
	v_add_co_u32_e32 v4, vcc, s4, v2
	s_movk_i32 s4, 0x2000
	s_nop 0
	v_addc_co_u32_e32 v5, vcc, 0, v3, vcc
	v_add_co_u32_e32 v6, vcc, s4, v2
	s_movk_i32 s4, 0x3000
	s_nop 0
	v_addc_co_u32_e32 v7, vcc, 0, v3, vcc
	global_load_dword v73, v[4:5], off offset:128
	global_load_dword v74, v[4:5], off offset:256
	global_load_dword v75, v[4:5], off offset:384
	global_load_dword v76, v[4:5], off offset:512
	global_load_dword v77, v[4:5], off offset:640
	global_load_dword v78, v[4:5], off offset:768
	global_load_dword v79, v[4:5], off offset:896
	global_load_dword v80, v[4:5], off offset:1024
	global_load_dword v81, v[4:5], off offset:1152
	global_load_dword v82, v[4:5], off offset:1280
	global_load_dword v83, v[4:5], off offset:1408
	global_load_dword v84, v[4:5], off offset:1536
	global_load_dword v85, v[4:5], off offset:1664
	global_load_dword v86, v[4:5], off offset:1792
	global_load_dword v87, v[4:5], off offset:1920
	global_load_dword v88, v[6:7], off offset:-4096
	global_load_dword v89, v[6:7], off
	global_load_dword v90, v[6:7], off offset:128
	global_load_dword v91, v[6:7], off offset:256
	global_load_dword v92, v[6:7], off offset:384
	global_load_dword v93, v[6:7], off offset:512
	global_load_dword v94, v[6:7], off offset:640
	global_load_dword v95, v[6:7], off offset:768
	global_load_dword v96, v[6:7], off offset:896
	global_load_dword v97, v[6:7], off offset:1024
	global_load_dword v98, v[6:7], off offset:1152
	global_load_dword v99, v[6:7], off offset:1280
	global_load_dword v100, v[6:7], off offset:1408
	global_load_dword v101, v[6:7], off offset:1536
	global_load_dword v102, v[6:7], off offset:1664
	global_load_dword v103, v[6:7], off offset:1792
	global_load_dword v104, v[6:7], off offset:1920
	v_add_co_u32_e32 v2, vcc, s4, v2
	v_and_b32_e32 v1, 7, v0
	s_nop 0
	v_addc_co_u32_e32 v3, vcc, 0, v3, vcc
	global_load_dword v105, v[2:3], off
	global_load_dword v106, v[2:3], off offset:128
	global_load_dword v107, v[2:3], off offset:256
	global_load_dword v108, v[2:3], off offset:384
	global_load_dword v109, v[2:3], off offset:512
	global_load_dword v110, v[2:3], off offset:640
	global_load_dword v111, v[2:3], off offset:768
	global_load_dword v112, v[2:3], off offset:896
	global_load_dword v113, v[2:3], off offset:1024
	global_load_dword v114, v[2:3], off offset:1152
	global_load_dword v115, v[2:3], off offset:1280
	global_load_dword v116, v[2:3], off offset:1408
	global_load_dword v117, v[2:3], off offset:1536
	global_load_dword v118, v[2:3], off offset:1664
	global_load_dword v119, v[2:3], off offset:1792
	global_load_dword v120, v[2:3], off offset:1920
	v_lshlrev_b32_e32 v121, 5, v1
	global_load_dwordx4 v[6:9], v121, s[8:9]
	global_load_dwordx4 v[2:5], v121, s[10:11]
	global_load_dwordx4 v[14:17], v121, s[8:9] offset:16
	global_load_dwordx4 v[10:13], v121, s[10:11] offset:16
	s_movk_i32 s8, 0x110
	s_waitcnt vmcnt(63)
	ds_write_b128 v122, v[22:25] offset:34816
	ds_write_b128 v122, v[26:29] offset:38976
	ds_write_b128 v122, v[30:33] offset:43136
	ds_write_b128 v122, v[34:37] offset:47296
	ds_write_b128 v122, v[38:41] offset:51456
	ds_write_b128 v122, v[42:45] offset:55616
	s_waitcnt vmcnt(63)
	ds_write_b128 v122, v[46:49] offset:59776
	s_waitcnt vmcnt(63)
	ds_write_b128 v122, v[50:53] offset:63936
	v_mul_u32_u24_e32 v22, 0x410, v56
	v_lshlrev_b32_e32 v23, 2, v57
	v_and_b32_e32 v24, 32, v0
	v_add3_u32 v38, v22, v23, v24
	s_waitcnt lgkmcnt(0)
	ds_read_b128 v[22:25], v38 offset:34832
	ds_read_b128 v[26:29], v38 offset:34816
	ds_read_b128 v[30:33], v38 offset:34880
	ds_read_b128 v[34:37], v38 offset:34896
	s_waitcnt lgkmcnt(3)
	v_cvt_pk_f16_f32 v25, v24, v25
	v_cvt_pk_f16_f32 v24, v22, v23
	s_waitcnt lgkmcnt(2)
	v_cvt_pk_f16_f32 v23, v28, v29
	v_cvt_pk_f16_f32 v22, v26, v27
	s_waitcnt vmcnt(53)
	v_cvt_pk_f16_f32 v29, v69, v71
	v_cvt_pk_f16_f32 v28, v19, v67
	v_cvt_pk_f16_f32 v27, v62, v64
	v_cvt_pk_f16_f32 v26, v58, v60
	v_lshlrev_b32_e32 v19, 2, v55
	s_nop 0
	v_mfma_f32_32x32x16_f16 a[0:15], v[22:25], v[26:29], 0
	s_waitcnt vmcnt(52)
	v_cvt_pk_f16_f32 v29, v70, v72
	v_cvt_pk_f16_f32 v28, v66, v68
	v_cvt_pk_f16_f32 v27, v63, v65
	v_cvt_pk_f16_f32 v26, v59, v61
	s_nop 1
	v_mfma_f32_32x32x16_f16 a[16:31], v[22:25], v[26:29], 0
	s_waitcnt lgkmcnt(0)
	v_cvt_pk_f16_f32 v25, v36, v37
	v_cvt_pk_f16_f32 v24, v34, v35
	v_cvt_pk_f16_f32 v23, v32, v33
	v_cvt_pk_f16_f32 v22, v30, v31
	ds_read_b128 v[30:33], v38 offset:34944
	ds_read_b128 v[34:37], v38 offset:34960
	s_waitcnt vmcnt(38)
	v_cvt_pk_f16_f32 v29, v84, v86
	v_cvt_pk_f16_f32 v28, v80, v82
	v_cvt_pk_f16_f32 v27, v76, v78
	s_waitcnt vmcnt(36)
	v_cvt_pk_f16_f32 v26, v88, v74
	s_nop 1
	v_mfma_f32_32x32x16_f16 a[0:15], v[22:25], v[26:29], a[0:15]
	v_cvt_pk_f16_f32 v29, v85, v87
	v_cvt_pk_f16_f32 v28, v81, v83
	v_cvt_pk_f16_f32 v27, v77, v79
	v_cvt_pk_f16_f32 v26, v73, v75
	s_nop 1
	v_mfma_f32_32x32x16_f16 a[16:31], v[22:25], v[26:29], a[16:31]
	s_waitcnt lgkmcnt(0)
	v_cvt_pk_f16_f32 v25, v36, v37
	v_cvt_pk_f16_f32 v24, v34, v35
	v_cvt_pk_f16_f32 v23, v32, v33
	v_cvt_pk_f16_f32 v22, v30, v31
	ds_read_b128 v[30:33], v38 offset:35008
	ds_read_b128 v[34:37], v38 offset:35024
	s_waitcnt vmcnt(21)
	v_cvt_pk_f16_f32 v29, v101, v103
	v_cvt_pk_f16_f32 v28, v97, v99
	v_cvt_pk_f16_f32 v27, v93, v95
	v_cvt_pk_f16_f32 v26, v89, v91
	s_nop 1
	v_mfma_f32_32x32x16_f16 a[0:15], v[22:25], v[26:29], a[0:15]
	s_waitcnt vmcnt(20)
	v_cvt_pk_f16_f32 v29, v102, v104
	v_cvt_pk_f16_f32 v28, v98, v100
	v_cvt_pk_f16_f32 v27, v94, v96
	v_cvt_pk_f16_f32 v26, v90, v92
	s_nop 1
	v_mfma_f32_32x32x16_f16 a[16:31], v[22:25], v[26:29], a[16:31]
	s_waitcnt lgkmcnt(0)
	v_cvt_pk_f16_f32 v25, v36, v37
	v_cvt_pk_f16_f32 v24, v34, v35
	v_cvt_pk_f16_f32 v23, v32, v33
	v_cvt_pk_f16_f32 v22, v30, v31
	s_waitcnt vmcnt(5)
	v_cvt_pk_f16_f32 v29, v117, v119
	v_cvt_pk_f16_f32 v28, v113, v115
	v_cvt_pk_f16_f32 v27, v109, v111
	v_cvt_pk_f16_f32 v26, v105, v107
	s_nop 1
	v_mfma_f32_32x32x16_f16 a[0:15], v[22:25], v[26:29], a[0:15]
	s_waitcnt vmcnt(4)
	v_cvt_pk_f16_f32 v29, v118, v120
	v_cvt_pk_f16_f32 v28, v114, v116
	v_cvt_pk_f16_f32 v27, v110, v112
	v_cvt_pk_f16_f32 v26, v106, v108
	s_nop 1
	v_mfma_f32_32x32x16_f16 a[16:31], v[22:25], v[26:29], a[16:31]
	v_lshl_or_b32 v22, v54, 5, v19
	v_mul_u32_u24_e32 v22, 0x44, v22
	v_lshl_add_u32 v22, v22, 2, v18
	s_nop 0
	ds_write_b32 v22, a0
	s_nop 6
	ds_write_b32 v22, a16 offset:128
	ds_write_b32 v22, a1 offset:272
	ds_write_b32 v22, a17 offset:400
	ds_write_b32 v22, a2 offset:544
	ds_write_b32 v22, a18 offset:672
	ds_write_b32 v22, a3 offset:816
	ds_write_b32 v22, a19 offset:944
	ds_write_b32 v22, a4 offset:2176
	ds_write_b32 v22, a20 offset:2304
	ds_write_b32 v22, a5 offset:2448
	ds_write_b32 v22, a21 offset:2576
	ds_write_b32 v22, a6 offset:2720
	ds_write_b32 v22, a22 offset:2848
	ds_write_b32 v22, a7 offset:2992
	ds_write_b32 v22, a23 offset:3120
	ds_write_b32 v22, a8 offset:4352
	ds_write_b32 v22, a24 offset:4480
	ds_write_b32 v22, a9 offset:4624
	ds_write_b32 v22, a25 offset:4752
	ds_write_b32 v22, a10 offset:4896
	ds_write_b32 v22, a26 offset:5024
	ds_write_b32 v22, a11 offset:5168
	ds_write_b32 v22, a27 offset:5296
	ds_write_b32 v22, a12 offset:6528
	ds_write_b32 v22, a28 offset:6656
	ds_write_b32 v22, a13 offset:6800
	ds_write_b32 v22, a29 offset:6928
	ds_write_b32 v22, a14 offset:7072
	ds_write_b32 v22, a30 offset:7200
	ds_write_b32 v22, a15 offset:7344
	ds_write_b32 v22, a31 offset:7472
	v_lshrrev_b32_e32 v22, 3, v0
	v_mad_u32_u24 v23, v22, s8, v121
	s_waitcnt lgkmcnt(0)
	s_barrier
	ds_read_b128 v[24:27], v23
	ds_read_b128 v[28:31], v23 offset:16
	ds_read_b128 v[32:35], v23 offset:8704
	s_waitcnt lgkmcnt(2)
	v_pk_add_f32 v[36:37], v[26:27], 0 op_sel_hi:[1,0]
	v_pk_add_f32 v[38:39], v[24:25], 0 op_sel_hi:[1,0]
	ds_read_b128 v[24:27], v23 offset:8720
	s_waitcnt lgkmcnt(2)
	v_pk_add_f32 v[40:41], v[30:31], 0 op_sel_hi:[1,0]
	v_pk_add_f32 v[42:43], v[28:29], 0 op_sel_hi:[1,0]
	ds_read_b128 v[28:31], v23 offset:17408
	s_waitcnt lgkmcnt(2)
	v_pk_add_f32 v[34:35], v[36:37], v[34:35]
	v_pk_add_f32 v[36:37], v[38:39], v[32:33]
	s_waitcnt lgkmcnt(1)
	v_pk_add_f32 v[38:39], v[40:41], v[26:27]
	v_pk_add_f32 v[40:41], v[42:43], v[24:25]
	ds_read_b128 v[24:27], v23 offset:17424
	s_waitcnt lgkmcnt(1)
	v_pk_add_f32 v[42:43], v[34:35], v[30:31]
	ds_read_b128 v[30:33], v23 offset:26112
	v_pk_add_f32 v[28:29], v[36:37], v[28:29]
	ds_read_b128 v[34:37], v23 offset:26128
	s_waitcnt lgkmcnt(2)
	v_pk_add_f32 v[40:41], v[40:41], v[24:25]
	v_pk_add_f32 v[38:39], v[38:39], v[26:27]
	s_waitcnt lgkmcnt(1)
	v_pk_add_f32 v[24:25], v[28:29], v[30:31]
	v_pk_add_f32 v[26:27], v[42:43], v[32:33]
	s_waitcnt lgkmcnt(0)
	v_pk_add_f32 v[28:29], v[40:41], v[34:35]
	v_pk_add_f32 v[30:31], v[38:39], v[36:37]
	s_waitcnt vmcnt(0)
	v_mul_f32_e32 v10, v28, v10
	v_fmac_f32_e32 v10, v24, v2
	v_mul_f32_e32 v14, v28, v14
	v_add_f32_e32 v2, 0, v10
	v_mul_f32_e32 v10, v29, v15
	v_fmac_f32_e32 v14, v24, v6
	v_fmac_f32_e32 v10, v25, v7
	v_mul_f32_e32 v7, v29, v11
	v_add_f32_e32 v6, 0, v14
	v_fmac_f32_e32 v7, v25, v3
	v_mul_f32_e32 v3, v30, v16
	v_add_f32_e32 v6, v6, v10
	v_fmac_f32_e32 v3, v26, v8
	v_add_f32_e32 v3, v6, v3
	v_mul_f32_e32 v6, v30, v12
	v_fmac_f32_e32 v6, v26, v4
	v_mul_f32_e32 v4, v31, v17
	v_fmac_f32_e32 v4, v27, v9
	v_add_f32_e32 v2, v2, v7
	v_add_f32_e32 v3, v3, v4
	v_mul_f32_e32 v4, v31, v13
	v_add_f32_e32 v2, v2, v6
	v_fmac_f32_e32 v4, v27, v5
	v_add_f32_e32 v2, v2, v4
	ds_write_b128 v23, v[24:27]
	ds_write_b128 v23, v[28:31] offset:16
	s_nop 1
	v_add_f32_dpp v3, v3, v3 quad_perm:[1,0,3,2] row_mask:0xf bank_mask:0xf
	v_add_f32_dpp v6, v2, v2 quad_perm:[1,0,3,2] row_mask:0xf bank_mask:0xf
	s_nop 1
	v_add_f32_dpp v3, v3, v3 quad_perm:[2,3,0,1] row_mask:0xf bank_mask:0xf
	v_add_f32_dpp v6, v6, v6 quad_perm:[2,3,0,1] row_mask:0xf bank_mask:0xf
	s_nop 1
	v_add_f32_dpp v2, v3, v3 row_half_mirror row_mask:0xf bank_mask:0xf
	v_add_f32_dpp v3, v6, v6 row_half_mirror row_mask:0xf bank_mask:0xf
	v_cmp_eq_u32_e32 vcc, 0, v1
	s_and_saveexec_b64 s[6:7], vcc
	s_cbranch_execz .LBB0_2
	v_mul_f32_e32 v4, 0x3f7d70a4, v3
	v_mul_f32_e32 v4, 0x3fb8aa3b, v4
	v_mul_f32_e32 v3, 0x3c23d70a, v3
	v_exp_f32_e32 v4, v4
	v_mul_f32_e32 v3, 0x3fb8aa3b, v3
	v_exp_f32_e32 v3, v3
	v_lshlrev_b32_e32 v5, 2, v22
	v_or_b32_e32 v6, 0x10a80, v5
	v_mul_f32_e32 v2, 0xbf7d70a4, v2
	ds_write_b32 v6, v4
	v_or_b32_e32 v4, 0x10a00, v5
	v_mul_f32_e32 v2, 0x3fb8aa3b, v2
	ds_write_b32 v4, v3
	v_exp_f32_e32 v4, v2
	v_add_u32_e32 v2, s3, v22
	v_ashrrev_i32_e32 v3, 31, v2
	v_lshl_add_u64 v[2:3], v[2:3], 2, s[18:19]
	global_store_dword v[2:3], v4, off sc1
